# expert-weight conversion rewritten: LDS-free 128x32 tiles, in-register 4x4 transpose, full 128-byte line reads and fp8 writes
# speedup vs baseline: 1.0191x; 1.0191x over previous
.LBB0_332:
	s_or_b64 exec, exec, s[4:5]
	v_mov_b32_e32 v1, 0x2000
	v_mov_b32_e32 v2, 1
	s_waitcnt vmcnt(0)
	buffer_inv sc1
	global_atomic_add v1, v2, s[2:3] offset:1024
	s_waitcnt vmcnt(0)

.Lconv_entry:
	v_readlane_b32 s0, v255, 7
	s_and_b32 s1, s76, 31
	s_lshl_b32 s1, s1, 3
	s_lshr_b32 s2, s76, 5
	s_or_b32 s1, s1, s2
	s_mul_i32 s2, s1, 0xb2
	s_sub_u32 s3, s1, 0x90
	s_mul_i32 s3, s3, 0xd2
	s_add_u32 s3, s3, 0x6420
	s_movk_i32 s15, 0xd2
	s_cmp_lt_u32 s1, 0x90
	s_cselect_b32 s14, s2, s3
	s_cselect_b32 s15, 0xb2, s15
	s_add_u32 s15, s15, s14
	s_add_u32 s14, s14, s0
	v_lshrrev_b32_e32 v2, 3, v254
	v_lshlrev_b32_e32 v2, 4, v2
	v_and_b32_e32 v3, 7, v254
	v_lshlrev_b32_e32 v4, 4, v3
	v_lshlrev_b32_e32 v3, 2, v3
	v_mov_b32_e32 v5, 0x43e00000
	s_mov_b32 s25, 0xc3e00000
	s_cmp_lt_u32 s14, s15
	s_cbranch_scc0 .Lconv_done
	s_cmp_lt_u32 s14, 0x8000
	s_cbranch_scc0 .Lconv_dn_p
	s_lshr_b32 s0, s14, 14
	s_and_b32 s1, s14, 0x3fff
	s_cmp_eq_u32 s0, 0
	s_cselect_b32 s16, s36, s38
	s_cselect_b32 s17, s37, s39
	s_lshr_b32 s2, s1, 8
	s_and_b32 s3, s1, 0xff
	s_lshr_b32 s1, s3, 4
	s_and_b32 s3, s3, 15
	s_lshl_b32 s10, s2, 22
	s_lshl_b32 s11, s1, 18
	s_add_u32 s10, s10, s11
	s_lshl_b32 s11, s3, 7
	s_add_u32 s10, s10, s11
	s_add_u32 s16, s16, s10
	s_addc_u32 s17, s17, 0
	s_movk_i32 s18, 0x800
	s_lshl_b32 s10, s2, 10
	s_lshr_b32 s11, s3, 2
	s_lshl_b32 s11, s11, 8
	s_add_u32 s10, s10, s11
	s_lshl_b32 s11, s0, 7
	s_add_u32 s10, s10, s11
	s_and_b32 s11, s3, 3
	s_lshl_b32 s11, s11, 5
	s_add_u32 s10, s10, s11
	s_lshl_b32 s10, s10, 11
	s_lshl_b32 s11, s1, 7
	s_add_u32 s10, s10, s11
	s_add_u32 s20, s50, 0x1c200000
	s_addc_u32 s21, s51, 0
	s_add_u32 s20, s20, s10
	s_addc_u32 s21, s21, 0
	s_movk_i32 s19, 0x800
	s_branch .Lconv_ad_p
.Lconv_dn_p:
	s_sub_u32 s1, s14, 0x8000
	s_lshr_b32 s2, s1, 8
	s_and_b32 s3, s1, 0xff
	s_lshr_b32 s1, s3, 6
	s_and_b32 s3, s3, 63
	s_lshl_b32 s10, s2, 22
	s_lshl_b32 s11, s1, 20
	s_add_u32 s10, s10, s11
	s_lshl_b32 s11, s3, 7
	s_add_u32 s10, s10, s11
	s_add_u32 s16, s40, s10
	s_addc_u32 s17, s41, 0
	s_movk_i32 s18, 0x2000
	s_lshl_b32 s10, s2, 11
	s_lshl_b32 s11, s3, 5
	s_add_u32 s10, s10, s11
	s_lshl_b32 s10, s10, 9
	s_lshl_b32 s11, s1, 7
	s_add_u32 s10, s10, s11
	s_add_u32 s20, s50, 0x2c600000
	s_addc_u32 s21, s51, 0
	s_add_u32 s20, s20, s10
	s_addc_u32 s21, s21, 0
	s_movk_i32 s19, 0x200
.Lconv_ad_p:
	v_mad_u32_u24 v6, v2, s18, v4
	v_mad_u32_u24 v7, v3, s19, v2
	global_load_dwordx4 v[16:19], v6, s[16:17] nt
	s_add_u32 s16, s16, s18
	s_addc_u32 s17, s17, 0
	global_load_dwordx4 v[20:23], v6, s[16:17] nt
	s_add_u32 s16, s16, s18
	s_addc_u32 s17, s17, 0
	global_load_dwordx4 v[24:27], v6, s[16:17] nt
	s_add_u32 s16, s16, s18
	s_addc_u32 s17, s17, 0
	global_load_dwordx4 v[28:31], v6, s[16:17] nt
	s_add_u32 s16, s16, s18
	s_addc_u32 s17, s17, 0
	global_load_dwordx4 v[32:35], v6, s[16:17] nt
	s_add_u32 s16, s16, s18
	s_addc_u32 s17, s17, 0
	global_load_dwordx4 v[36:39], v6, s[16:17] nt
	s_add_u32 s16, s16, s18
	s_addc_u32 s17, s17, 0
	global_load_dwordx4 v[40:43], v6, s[16:17] nt
	s_add_u32 s16, s16, s18
	s_addc_u32 s17, s17, 0
	global_load_dwordx4 v[44:47], v6, s[16:17] nt
	s_add_u32 s16, s16, s18
	s_addc_u32 s17, s17, 0
	global_load_dwordx4 v[48:51], v6, s[16:17] nt
	s_add_u32 s16, s16, s18
	s_addc_u32 s17, s17, 0
	global_load_dwordx4 v[52:55], v6, s[16:17] nt
	s_add_u32 s16, s16, s18
	s_addc_u32 s17, s17, 0
	global_load_dwordx4 v[56:59], v6, s[16:17] nt
	s_add_u32 s16, s16, s18
	s_addc_u32 s17, s17, 0
	global_load_dwordx4 v[60:63], v6, s[16:17] nt
	s_add_u32 s16, s16, s18
	s_addc_u32 s17, s17, 0
	global_load_dwordx4 v[64:67], v6, s[16:17] nt
	s_add_u32 s16, s16, s18
	s_addc_u32 s17, s17, 0
	global_load_dwordx4 v[68:71], v6, s[16:17] nt
	s_add_u32 s16, s16, s18
	s_addc_u32 s17, s17, 0
	global_load_dwordx4 v[72:75], v6, s[16:17] nt
	s_add_u32 s16, s16, s18
	s_addc_u32 s17, s17, 0
	global_load_dwordx4 v[76:79], v6, s[16:17] nt
.Lconv_loop:
	s_add_u32 s27, s14, 8
	s_cmp_lt_u32 s27, s15
	s_cbranch_scc0 .Lconv_tailA
	s_cmp_lt_u32 s27, 0x8000
	s_cbranch_scc0 .Lconv_dn_b
	s_lshr_b32 s0, s27, 14
	s_and_b32 s1, s27, 0x3fff
	s_cmp_eq_u32 s0, 0
	s_cselect_b32 s16, s36, s38
	s_cselect_b32 s17, s37, s39
	s_lshr_b32 s2, s1, 8
	s_and_b32 s3, s1, 0xff
	s_lshr_b32 s1, s3, 4
	s_and_b32 s3, s3, 15
	s_lshl_b32 s10, s2, 22
	s_lshl_b32 s11, s1, 18
	s_add_u32 s10, s10, s11
	s_lshl_b32 s11, s3, 7
	s_add_u32 s10, s10, s11
	s_add_u32 s16, s16, s10
	s_addc_u32 s17, s17, 0
	s_movk_i32 s18, 0x800
	s_lshl_b32 s10, s2, 10
	s_lshr_b32 s11, s3, 2
	s_lshl_b32 s11, s11, 8
	s_add_u32 s10, s10, s11
	s_lshl_b32 s11, s0, 7
	s_add_u32 s10, s10, s11
	s_and_b32 s11, s3, 3
	s_lshl_b32 s11, s11, 5
	s_add_u32 s10, s10, s11
	s_lshl_b32 s10, s10, 11
	s_lshl_b32 s11, s1, 7
	s_add_u32 s10, s10, s11
	s_add_u32 s22, s50, 0x1c200000
	s_addc_u32 s23, s51, 0
	s_add_u32 s22, s22, s10
	s_addc_u32 s23, s23, 0
	s_movk_i32 s24, 0x800
	s_branch .Lconv_ad_b
.Lconv_dn_b:
	s_sub_u32 s1, s27, 0x8000
	s_lshr_b32 s2, s1, 8
	s_and_b32 s3, s1, 0xff
	s_lshr_b32 s1, s3, 6
	s_and_b32 s3, s3, 63
	s_lshl_b32 s10, s2, 22
	s_lshl_b32 s11, s1, 20
	s_add_u32 s10, s10, s11
	s_lshl_b32 s11, s3, 7
	s_add_u32 s10, s10, s11
	s_add_u32 s16, s40, s10
	s_addc_u32 s17, s41, 0
	s_movk_i32 s18, 0x2000
	s_lshl_b32 s10, s2, 11
	s_lshl_b32 s11, s3, 5
	s_add_u32 s10, s10, s11
	s_lshl_b32 s10, s10, 9
	s_lshl_b32 s11, s1, 7
	s_add_u32 s10, s10, s11
	s_add_u32 s22, s50, 0x2c600000
	s_addc_u32 s23, s51, 0
	s_add_u32 s22, s22, s10
	s_addc_u32 s23, s23, 0
	s_movk_i32 s24, 0x200
.Lconv_ad_b:
	v_mad_u32_u24 v6, v2, s18, v4
	v_mad_u32_u24 v8, v3, s24, v2
	global_load_dwordx4 v[80:83], v6, s[16:17] nt
	s_add_u32 s16, s16, s18
	s_addc_u32 s17, s17, 0
	global_load_dwordx4 v[84:87], v6, s[16:17] nt
	s_add_u32 s16, s16, s18
	s_addc_u32 s17, s17, 0
	global_load_dwordx4 v[88:91], v6, s[16:17] nt
	s_add_u32 s16, s16, s18
	s_addc_u32 s17, s17, 0
	global_load_dwordx4 v[92:95], v6, s[16:17] nt
	s_add_u32 s16, s16, s18
	s_addc_u32 s17, s17, 0
	global_load_dwordx4 v[96:99], v6, s[16:17] nt
	s_add_u32 s16, s16, s18
	s_addc_u32 s17, s17, 0
	global_load_dwordx4 v[100:103], v6, s[16:17] nt
	s_add_u32 s16, s16, s18
	s_addc_u32 s17, s17, 0
	global_load_dwordx4 v[104:107], v6, s[16:17] nt
	s_add_u32 s16, s16, s18
	s_addc_u32 s17, s17, 0
	global_load_dwordx4 v[108:111], v6, s[16:17] nt
	s_add_u32 s16, s16, s18
	s_addc_u32 s17, s17, 0
	global_load_dwordx4 v[112:115], v6, s[16:17] nt
	s_add_u32 s16, s16, s18
	s_addc_u32 s17, s17, 0
	global_load_dwordx4 v[116:119], v6, s[16:17] nt
	s_add_u32 s16, s16, s18
	s_addc_u32 s17, s17, 0
	global_load_dwordx4 v[120:123], v6, s[16:17] nt
	s_add_u32 s16, s16, s18
	s_addc_u32 s17, s17, 0
	global_load_dwordx4 v[124:127], v6, s[16:17] nt
	s_add_u32 s16, s16, s18
	s_addc_u32 s17, s17, 0
	global_load_dwordx4 v[128:131], v6, s[16:17] nt
	s_add_u32 s16, s16, s18
	s_addc_u32 s17, s17, 0
	global_load_dwordx4 v[132:135], v6, s[16:17] nt
	s_add_u32 s16, s16, s18
	s_addc_u32 s17, s17, 0
	global_load_dwordx4 v[136:139], v6, s[16:17] nt
	s_add_u32 s16, s16, s18
	s_addc_u32 s17, s17, 0
	global_load_dwordx4 v[140:143], v6, s[16:17] nt
	s_waitcnt vmcnt(16)
	v_mul_f32_e32 v160, 0x41800000, v16
	v_mul_f32_e32 v161, 0x41800000, v20
	v_mul_f32_e32 v162, 0x41800000, v24
	v_mul_f32_e32 v163, 0x41800000, v28
	v_med3_f32 v160, v160, s25, v5
	v_med3_f32 v161, v161, s25, v5
	v_med3_f32 v162, v162, s25, v5
	v_med3_f32 v163, v163, s25, v5
	v_cvt_pk_fp8_f32 v144, v160, v161
	v_cvt_pk_fp8_f32 v144, v162, v163 op_sel:[0,0,1]
	v_mul_f32_e32 v164, 0x41800000, v32
	v_mul_f32_e32 v165, 0x41800000, v36
	v_mul_f32_e32 v166, 0x41800000, v40
	v_mul_f32_e32 v167, 0x41800000, v44
	v_med3_f32 v164, v164, s25, v5
	v_med3_f32 v165, v165, s25, v5
	v_med3_f32 v166, v166, s25, v5
	v_med3_f32 v167, v167, s25, v5
	v_cvt_pk_fp8_f32 v145, v164, v165
	v_cvt_pk_fp8_f32 v145, v166, v167 op_sel:[0,0,1]
	v_mul_f32_e32 v160, 0x41800000, v48
	v_mul_f32_e32 v161, 0x41800000, v52
	v_mul_f32_e32 v162, 0x41800000, v56
	v_mul_f32_e32 v163, 0x41800000, v60
	v_med3_f32 v160, v160, s25, v5
	v_med3_f32 v161, v161, s25, v5
	v_med3_f32 v162, v162, s25, v5
	v_med3_f32 v163, v163, s25, v5
	v_cvt_pk_fp8_f32 v146, v160, v161
	v_cvt_pk_fp8_f32 v146, v162, v163 op_sel:[0,0,1]
	v_mul_f32_e32 v164, 0x41800000, v64
	v_mul_f32_e32 v165, 0x41800000, v68
	v_mul_f32_e32 v166, 0x41800000, v72
	v_mul_f32_e32 v167, 0x41800000, v76
	v_med3_f32 v164, v164, s25, v5
	v_med3_f32 v165, v165, s25, v5
	v_med3_f32 v166, v166, s25, v5
	v_med3_f32 v167, v167, s25, v5
	v_cvt_pk_fp8_f32 v147, v164, v165
	v_cvt_pk_fp8_f32 v147, v166, v167 op_sel:[0,0,1]
	s_nop 0
	global_store_dwordx4 v7, v[144:147], s[20:21] nt
	s_add_u32 s20, s20, s19
	s_addc_u32 s21, s21, 0
	v_mul_f32_e32 v160, 0x41800000, v17
	v_mul_f32_e32 v161, 0x41800000, v21
	v_mul_f32_e32 v162, 0x41800000, v25
	v_mul_f32_e32 v163, 0x41800000, v29
	v_med3_f32 v160, v160, s25, v5
	v_med3_f32 v161, v161, s25, v5
	v_med3_f32 v162, v162, s25, v5
	v_med3_f32 v163, v163, s25, v5
	v_cvt_pk_fp8_f32 v148, v160, v161
	v_cvt_pk_fp8_f32 v148, v162, v163 op_sel:[0,0,1]
	v_mul_f32_e32 v164, 0x41800000, v33
	v_mul_f32_e32 v165, 0x41800000, v37
	v_mul_f32_e32 v166, 0x41800000, v41
	v_mul_f32_e32 v167, 0x41800000, v45
	v_med3_f32 v164, v164, s25, v5
	v_med3_f32 v165, v165, s25, v5
	v_med3_f32 v166, v166, s25, v5
	v_med3_f32 v167, v167, s25, v5
	v_cvt_pk_fp8_f32 v149, v164, v165
	v_cvt_pk_fp8_f32 v149, v166, v167 op_sel:[0,0,1]
	v_mul_f32_e32 v160, 0x41800000, v49
	v_mul_f32_e32 v161, 0x41800000, v53
	v_mul_f32_e32 v162, 0x41800000, v57
	v_mul_f32_e32 v163, 0x41800000, v61
	v_med3_f32 v160, v160, s25, v5
	v_med3_f32 v161, v161, s25, v5
	v_med3_f32 v162, v162, s25, v5
	v_med3_f32 v163, v163, s25, v5
	v_cvt_pk_fp8_f32 v150, v160, v161
	v_cvt_pk_fp8_f32 v150, v162, v163 op_sel:[0,0,1]
	v_mul_f32_e32 v164, 0x41800000, v65
	v_mul_f32_e32 v165, 0x41800000, v69
	v_mul_f32_e32 v166, 0x41800000, v73
	v_mul_f32_e32 v167, 0x41800000, v77
	v_med3_f32 v164, v164, s25, v5
	v_med3_f32 v165, v165, s25, v5
	v_med3_f32 v166, v166, s25, v5
	v_med3_f32 v167, v167, s25, v5
	v_cvt_pk_fp8_f32 v151, v164, v165
	v_cvt_pk_fp8_f32 v151, v166, v167 op_sel:[0,0,1]
	s_nop 0
	global_store_dwordx4 v7, v[148:151], s[20:21] nt
	s_add_u32 s20, s20, s19
	s_addc_u32 s21, s21, 0
	v_mul_f32_e32 v160, 0x41800000, v18
	v_mul_f32_e32 v161, 0x41800000, v22
	v_mul_f32_e32 v162, 0x41800000, v26
	v_mul_f32_e32 v163, 0x41800000, v30
	v_med3_f32 v160, v160, s25, v5
	v_med3_f32 v161, v161, s25, v5
	v_med3_f32 v162, v162, s25, v5
	v_med3_f32 v163, v163, s25, v5
	v_cvt_pk_fp8_f32 v152, v160, v161
	v_cvt_pk_fp8_f32 v152, v162, v163 op_sel:[0,0,1]
	v_mul_f32_e32 v164, 0x41800000, v34
	v_mul_f32_e32 v165, 0x41800000, v38
	v_mul_f32_e32 v166, 0x41800000, v42
	v_mul_f32_e32 v167, 0x41800000, v46
	v_med3_f32 v164, v164, s25, v5
	v_med3_f32 v165, v165, s25, v5
	v_med3_f32 v166, v166, s25, v5
	v_med3_f32 v167, v167, s25, v5
	v_cvt_pk_fp8_f32 v153, v164, v165
	v_cvt_pk_fp8_f32 v153, v166, v167 op_sel:[0,0,1]
	v_mul_f32_e32 v160, 0x41800000, v50
	v_mul_f32_e32 v161, 0x41800000, v54
	v_mul_f32_e32 v162, 0x41800000, v58
	v_mul_f32_e32 v163, 0x41800000, v62
	v_med3_f32 v160, v160, s25, v5
	v_med3_f32 v161, v161, s25, v5
	v_med3_f32 v162, v162, s25, v5
	v_med3_f32 v163, v163, s25, v5
	v_cvt_pk_fp8_f32 v154, v160, v161
	v_cvt_pk_fp8_f32 v154, v162, v163 op_sel:[0,0,1]
	v_mul_f32_e32 v164, 0x41800000, v66
	v_mul_f32_e32 v165, 0x41800000, v70
	v_mul_f32_e32 v166, 0x41800000, v74
	v_mul_f32_e32 v167, 0x41800000, v78
	v_med3_f32 v164, v164, s25, v5
	v_med3_f32 v165, v165, s25, v5
	v_med3_f32 v166, v166, s25, v5
	v_med3_f32 v167, v167, s25, v5
	v_cvt_pk_fp8_f32 v155, v164, v165
	v_cvt_pk_fp8_f32 v155, v166, v167 op_sel:[0,0,1]
	s_nop 0
	global_store_dwordx4 v7, v[152:155], s[20:21] nt
	s_add_u32 s20, s20, s19
	s_addc_u32 s21, s21, 0
	v_mul_f32_e32 v160, 0x41800000, v19
	v_mul_f32_e32 v161, 0x41800000, v23
	v_mul_f32_e32 v162, 0x41800000, v27
	v_mul_f32_e32 v163, 0x41800000, v31
	v_med3_f32 v160, v160, s25, v5
	v_med3_f32 v161, v161, s25, v5
	v_med3_f32 v162, v162, s25, v5
	v_med3_f32 v163, v163, s25, v5
	v_cvt_pk_fp8_f32 v156, v160, v161
	v_cvt_pk_fp8_f32 v156, v162, v163 op_sel:[0,0,1]
	v_mul_f32_e32 v164, 0x41800000, v35
	v_mul_f32_e32 v165, 0x41800000, v39
	v_mul_f32_e32 v166, 0x41800000, v43
	v_mul_f32_e32 v167, 0x41800000, v47
	v_med3_f32 v164, v164, s25, v5
	v_med3_f32 v165, v165, s25, v5
	v_med3_f32 v166, v166, s25, v5
	v_med3_f32 v167, v167, s25, v5
	v_cvt_pk_fp8_f32 v157, v164, v165
	v_cvt_pk_fp8_f32 v157, v166, v167 op_sel:[0,0,1]
	v_mul_f32_e32 v160, 0x41800000, v51
	v_mul_f32_e32 v161, 0x41800000, v55
	v_mul_f32_e32 v162, 0x41800000, v59
	v_mul_f32_e32 v163, 0x41800000, v63
	v_med3_f32 v160, v160, s25, v5
	v_med3_f32 v161, v161, s25, v5
	v_med3_f32 v162, v162, s25, v5
	v_med3_f32 v163, v163, s25, v5
	v_cvt_pk_fp8_f32 v158, v160, v161
	v_cvt_pk_fp8_f32 v158, v162, v163 op_sel:[0,0,1]
	v_mul_f32_e32 v164, 0x41800000, v67
	v_mul_f32_e32 v165, 0x41800000, v71
	v_mul_f32_e32 v166, 0x41800000, v75
	v_mul_f32_e32 v167, 0x41800000, v79
	v_med3_f32 v164, v164, s25, v5
	v_med3_f32 v165, v165, s25, v5
	v_med3_f32 v166, v166, s25, v5
	v_med3_f32 v167, v167, s25, v5
	v_cvt_pk_fp8_f32 v159, v164, v165
	v_cvt_pk_fp8_f32 v159, v166, v167 op_sel:[0,0,1]
	s_nop 0
	global_store_dwordx4 v7, v[156:159], s[20:21] nt
	s_add_u32 s14, s27, 8
	s_cmp_lt_u32 s14, s15
	s_cbranch_scc0 .Lconv_tailB
	s_cmp_lt_u32 s14, 0x8000
	s_cbranch_scc0 .Lconv_dn_a
	s_lshr_b32 s0, s14, 14
	s_and_b32 s1, s14, 0x3fff
	s_cmp_eq_u32 s0, 0
	s_cselect_b32 s16, s36, s38
	s_cselect_b32 s17, s37, s39
	s_lshr_b32 s2, s1, 8
	s_and_b32 s3, s1, 0xff
	s_lshr_b32 s1, s3, 4
	s_and_b32 s3, s3, 15
	s_lshl_b32 s10, s2, 22
	s_lshl_b32 s11, s1, 18
	s_add_u32 s10, s10, s11
	s_lshl_b32 s11, s3, 7
	s_add_u32 s10, s10, s11
	s_add_u32 s16, s16, s10
	s_addc_u32 s17, s17, 0
	s_movk_i32 s18, 0x800
	s_lshl_b32 s10, s2, 10
	s_lshr_b32 s11, s3, 2
	s_lshl_b32 s11, s11, 8
	s_add_u32 s10, s10, s11
	s_lshl_b32 s11, s0, 7
	s_add_u32 s10, s10, s11
	s_and_b32 s11, s3, 3
	s_lshl_b32 s11, s11, 5
	s_add_u32 s10, s10, s11
	s_lshl_b32 s10, s10, 11
	s_lshl_b32 s11, s1, 7
	s_add_u32 s10, s10, s11
	s_add_u32 s20, s50, 0x1c200000
	s_addc_u32 s21, s51, 0
	s_add_u32 s20, s20, s10
	s_addc_u32 s21, s21, 0
	s_movk_i32 s19, 0x800
	s_branch .Lconv_ad_a

.Lconv_ad_a:
	v_mad_u32_u24 v6, v2, s18, v4
	v_mad_u32_u24 v7, v3, s19, v2
	global_load_dwordx4 v[16:19], v6, s[16:17] nt
	s_add_u32 s16, s16, s18
	s_addc_u32 s17, s17, 0
	global_load_dwordx4 v[20:23], v6, s[16:17] nt
	s_add_u32 s16, s16, s18
	s_addc_u32 s17, s17, 0
	global_load_dwordx4 v[24:27], v6, s[16:17] nt
	s_add_u32 s16, s16, s18
	s_addc_u32 s17, s17, 0
	global_load_dwordx4 v[28:31], v6, s[16:17] nt
	s_add_u32 s16, s16, s18
	s_addc_u32 s17, s17, 0
	global_load_dwordx4 v[32:35], v6, s[16:17] nt
	s_add_u32 s16, s16, s18
	s_addc_u32 s17, s17, 0
	global_load_dwordx4 v[36:39], v6, s[16:17] nt
	s_add_u32 s16, s16, s18
	s_addc_u32 s17, s17, 0
	global_load_dwordx4 v[40:43], v6, s[16:17] nt
	s_add_u32 s16, s16, s18
	s_addc_u32 s17, s17, 0
	global_load_dwordx4 v[44:47], v6, s[16:17] nt
	s_add_u32 s16, s16, s18
	s_addc_u32 s17, s17, 0
	global_load_dwordx4 v[48:51], v6, s[16:17] nt
	s_add_u32 s16, s16, s18
	s_addc_u32 s17, s17, 0
	global_load_dwordx4 v[52:55], v6, s[16:17] nt
	s_add_u32 s16, s16, s18
	s_addc_u32 s17, s17, 0
	global_load_dwordx4 v[56:59], v6, s[16:17] nt
	s_add_u32 s16, s16, s18
	s_addc_u32 s17, s17, 0
	global_load_dwordx4 v[60:63], v6, s[16:17] nt
	s_add_u32 s16, s16, s18
	s_addc_u32 s17, s17, 0
	global_load_dwordx4 v[64:67], v6, s[16:17] nt
	s_add_u32 s16, s16, s18
	s_addc_u32 s17, s17, 0
	global_load_dwordx4 v[68:71], v6, s[16:17] nt
	s_add_u32 s16, s16, s18
	s_addc_u32 s17, s17, 0
	global_load_dwordx4 v[72:75], v6, s[16:17] nt
	s_add_u32 s16, s16, s18
	s_addc_u32 s17, s17, 0
	global_load_dwordx4 v[76:79], v6, s[16:17] nt
	s_waitcnt vmcnt(20)
	v_mul_f32_e32 v160, 0x41800000, v80
	v_mul_f32_e32 v161, 0x41800000, v84
	v_mul_f32_e32 v162, 0x41800000, v88
	v_mul_f32_e32 v163, 0x41800000, v92
	v_med3_f32 v160, v160, s25, v5
	v_med3_f32 v161, v161, s25, v5
	v_med3_f32 v162, v162, s25, v5
	v_med3_f32 v163, v163, s25, v5
	v_cvt_pk_fp8_f32 v144, v160, v161
	v_cvt_pk_fp8_f32 v144, v162, v163 op_sel:[0,0,1]
	v_mul_f32_e32 v164, 0x41800000, v96
	v_mul_f32_e32 v165, 0x41800000, v100
	v_mul_f32_e32 v166, 0x41800000, v104
	v_mul_f32_e32 v167, 0x41800000, v108
	v_med3_f32 v164, v164, s25, v5
	v_med3_f32 v165, v165, s25, v5
	v_med3_f32 v166, v166, s25, v5
	v_med3_f32 v167, v167, s25, v5
	v_cvt_pk_fp8_f32 v145, v164, v165
	v_cvt_pk_fp8_f32 v145, v166, v167 op_sel:[0,0,1]
	v_mul_f32_e32 v160, 0x41800000, v112
	v_mul_f32_e32 v161, 0x41800000, v116
	v_mul_f32_e32 v162, 0x41800000, v120
	v_mul_f32_e32 v163, 0x41800000, v124
	v_med3_f32 v160, v160, s25, v5
	v_med3_f32 v161, v161, s25, v5
	v_med3_f32 v162, v162, s25, v5
	v_med3_f32 v163, v163, s25, v5
	v_cvt_pk_fp8_f32 v146, v160, v161
	v_cvt_pk_fp8_f32 v146, v162, v163 op_sel:[0,0,1]
	v_mul_f32_e32 v164, 0x41800000, v128
	v_mul_f32_e32 v165, 0x41800000, v132
	v_mul_f32_e32 v166, 0x41800000, v136
	v_mul_f32_e32 v167, 0x41800000, v140
	v_med3_f32 v164, v164, s25, v5
	v_med3_f32 v165, v165, s25, v5
	v_med3_f32 v166, v166, s25, v5
	v_med3_f32 v167, v167, s25, v5
	v_cvt_pk_fp8_f32 v147, v164, v165
	v_cvt_pk_fp8_f32 v147, v166, v167 op_sel:[0,0,1]
	s_nop 0
	global_store_dwordx4 v8, v[144:147], s[22:23] nt
	s_add_u32 s22, s22, s24
	s_addc_u32 s23, s23, 0
	v_mul_f32_e32 v160, 0x41800000, v81
	v_mul_f32_e32 v161, 0x41800000, v85
	v_mul_f32_e32 v162, 0x41800000, v89
	v_mul_f32_e32 v163, 0x41800000, v93
	v_med3_f32 v160, v160, s25, v5
	v_med3_f32 v161, v161, s25, v5
	v_med3_f32 v162, v162, s25, v5
	v_med3_f32 v163, v163, s25, v5
	v_cvt_pk_fp8_f32 v148, v160, v161
	v_cvt_pk_fp8_f32 v148, v162, v163 op_sel:[0,0,1]
	v_mul_f32_e32 v164, 0x41800000, v97
	v_mul_f32_e32 v165, 0x41800000, v101
	v_mul_f32_e32 v166, 0x41800000, v105
	v_mul_f32_e32 v167, 0x41800000, v109
	v_med3_f32 v164, v164, s25, v5
	v_med3_f32 v165, v165, s25, v5
	v_med3_f32 v166, v166, s25, v5
	v_med3_f32 v167, v167, s25, v5
	v_cvt_pk_fp8_f32 v149, v164, v165
	v_cvt_pk_fp8_f32 v149, v166, v167 op_sel:[0,0,1]
	v_mul_f32_e32 v160, 0x41800000, v113
	v_mul_f32_e32 v161, 0x41800000, v117
	v_mul_f32_e32 v162, 0x41800000, v121
	v_mul_f32_e32 v163, 0x41800000, v125
	v_med3_f32 v160, v160, s25, v5
	v_med3_f32 v161, v161, s25, v5
	v_med3_f32 v162, v162, s25, v5
	v_med3_f32 v163, v163, s25, v5
	v_cvt_pk_fp8_f32 v150, v160, v161
	v_cvt_pk_fp8_f32 v150, v162, v163 op_sel:[0,0,1]
	v_mul_f32_e32 v164, 0x41800000, v129
	v_mul_f32_e32 v165, 0x41800000, v133
	v_mul_f32_e32 v166, 0x41800000, v137
	v_mul_f32_e32 v167, 0x41800000, v141
	v_med3_f32 v164, v164, s25, v5
	v_med3_f32 v165, v165, s25, v5
	v_med3_f32 v166, v166, s25, v5
	v_med3_f32 v167, v167, s25, v5
	v_cvt_pk_fp8_f32 v151, v164, v165
	v_cvt_pk_fp8_f32 v151, v166, v167 op_sel:[0,0,1]
	s_nop 0
	global_store_dwordx4 v8, v[148:151], s[22:23] nt
	s_add_u32 s22, s22, s24
	s_addc_u32 s23, s23, 0
	v_mul_f32_e32 v160, 0x41800000, v82
	v_mul_f32_e32 v161, 0x41800000, v86
	v_mul_f32_e32 v162, 0x41800000, v90
	v_mul_f32_e32 v163, 0x41800000, v94
	v_med3_f32 v160, v160, s25, v5
	v_med3_f32 v161, v161, s25, v5
	v_med3_f32 v162, v162, s25, v5
	v_med3_f32 v163, v163, s25, v5
	v_cvt_pk_fp8_f32 v152, v160, v161
	v_cvt_pk_fp8_f32 v152, v162, v163 op_sel:[0,0,1]
	v_mul_f32_e32 v164, 0x41800000, v98
	v_mul_f32_e32 v165, 0x41800000, v102
	v_mul_f32_e32 v166, 0x41800000, v106
	v_mul_f32_e32 v167, 0x41800000, v110
	v_med3_f32 v164, v164, s25, v5
	v_med3_f32 v165, v165, s25, v5
	v_med3_f32 v166, v166, s25, v5
	v_med3_f32 v167, v167, s25, v5
	v_cvt_pk_fp8_f32 v153, v164, v165
	v_cvt_pk_fp8_f32 v153, v166, v167 op_sel:[0,0,1]
	v_mul_f32_e32 v160, 0x41800000, v114
	v_mul_f32_e32 v161, 0x41800000, v118
	v_mul_f32_e32 v162, 0x41800000, v122
	v_mul_f32_e32 v163, 0x41800000, v126
	v_med3_f32 v160, v160, s25, v5
	v_med3_f32 v161, v161, s25, v5
	v_med3_f32 v162, v162, s25, v5
	v_med3_f32 v163, v163, s25, v5
	v_cvt_pk_fp8_f32 v154, v160, v161
	v_cvt_pk_fp8_f32 v154, v162, v163 op_sel:[0,0,1]
	v_mul_f32_e32 v164, 0x41800000, v130
	v_mul_f32_e32 v165, 0x41800000, v134
	v_mul_f32_e32 v166, 0x41800000, v138
	v_mul_f32_e32 v167, 0x41800000, v142
	v_med3_f32 v164, v164, s25, v5
	v_med3_f32 v165, v165, s25, v5
	v_med3_f32 v166, v166, s25, v5
	v_med3_f32 v167, v167, s25, v5
	v_cvt_pk_fp8_f32 v155, v164, v165
	v_cvt_pk_fp8_f32 v155, v166, v167 op_sel:[0,0,1]
	s_nop 0
	global_store_dwordx4 v8, v[152:155], s[22:23] nt
	s_add_u32 s22, s22, s24
	s_addc_u32 s23, s23, 0
	v_mul_f32_e32 v160, 0x41800000, v83
	v_mul_f32_e32 v161, 0x41800000, v87
	v_mul_f32_e32 v162, 0x41800000, v91
	v_mul_f32_e32 v163, 0x41800000, v95
	v_med3_f32 v160, v160, s25, v5
	v_med3_f32 v161, v161, s25, v5
	v_med3_f32 v162, v162, s25, v5
	v_med3_f32 v163, v163, s25, v5
	v_cvt_pk_fp8_f32 v156, v160, v161
	v_cvt_pk_fp8_f32 v156, v162, v163 op_sel:[0,0,1]
	v_mul_f32_e32 v164, 0x41800000, v99
	v_mul_f32_e32 v165, 0x41800000, v103
	v_mul_f32_e32 v166, 0x41800000, v107
	v_mul_f32_e32 v167, 0x41800000, v111
	v_med3_f32 v164, v164, s25, v5
	v_med3_f32 v165, v165, s25, v5
	v_med3_f32 v166, v166, s25, v5
	v_med3_f32 v167, v167, s25, v5
	v_cvt_pk_fp8_f32 v157, v164, v165
	v_cvt_pk_fp8_f32 v157, v166, v167 op_sel:[0,0,1]
	v_mul_f32_e32 v160, 0x41800000, v115
	v_mul_f32_e32 v161, 0x41800000, v119
	v_mul_f32_e32 v162, 0x41800000, v123
	v_mul_f32_e32 v163, 0x41800000, v127
	v_med3_f32 v160, v160, s25, v5
	v_med3_f32 v161, v161, s25, v5
	v_med3_f32 v162, v162, s25, v5
	v_med3_f32 v163, v163, s25, v5
	v_cvt_pk_fp8_f32 v158, v160, v161
	v_cvt_pk_fp8_f32 v158, v162, v163 op_sel:[0,0,1]
	v_mul_f32_e32 v164, 0x41800000, v131
	v_mul_f32_e32 v165, 0x41800000, v135
	v_mul_f32_e32 v166, 0x41800000, v139
	v_mul_f32_e32 v167, 0x41800000, v143
	v_med3_f32 v164, v164, s25, v5
	v_med3_f32 v165, v165, s25, v5
	v_med3_f32 v166, v166, s25, v5
	v_med3_f32 v167, v167, s25, v5
	v_cvt_pk_fp8_f32 v159, v164, v165
	v_cvt_pk_fp8_f32 v159, v166, v167 op_sel:[0,0,1]
	s_nop 0
	global_store_dwordx4 v8, v[156:159], s[22:23] nt
	s_branch .Lconv_loop
.Lconv_tailA:
	s_waitcnt vmcnt(0)
	v_mul_f32_e32 v160, 0x41800000, v16
	v_mul_f32_e32 v161, 0x41800000, v20
	v_mul_f32_e32 v162, 0x41800000, v24
	v_mul_f32_e32 v163, 0x41800000, v28
	v_med3_f32 v160, v160, s25, v5
	v_med3_f32 v161, v161, s25, v5
	v_med3_f32 v162, v162, s25, v5
	v_med3_f32 v163, v163, s25, v5
	v_cvt_pk_fp8_f32 v144, v160, v161
	v_cvt_pk_fp8_f32 v144, v162, v163 op_sel:[0,0,1]
	v_mul_f32_e32 v164, 0x41800000, v32
	v_mul_f32_e32 v165, 0x41800000, v36
	v_mul_f32_e32 v166, 0x41800000, v40
	v_mul_f32_e32 v167, 0x41800000, v44
	v_med3_f32 v164, v164, s25, v5
	v_med3_f32 v165, v165, s25, v5
	v_med3_f32 v166, v166, s25, v5
	v_med3_f32 v167, v167, s25, v5
	v_cvt_pk_fp8_f32 v145, v164, v165
	v_cvt_pk_fp8_f32 v145, v166, v167 op_sel:[0,0,1]
	v_mul_f32_e32 v160, 0x41800000, v48
	v_mul_f32_e32 v161, 0x41800000, v52
	v_mul_f32_e32 v162, 0x41800000, v56
	v_mul_f32_e32 v163, 0x41800000, v60
	v_med3_f32 v160, v160, s25, v5
	v_med3_f32 v161, v161, s25, v5
	v_med3_f32 v162, v162, s25, v5
	v_med3_f32 v163, v163, s25, v5
	v_cvt_pk_fp8_f32 v146, v160, v161
	v_cvt_pk_fp8_f32 v146, v162, v163 op_sel:[0,0,1]
	v_mul_f32_e32 v164, 0x41800000, v64
	v_mul_f32_e32 v165, 0x41800000, v68
	v_mul_f32_e32 v166, 0x41800000, v72
	v_mul_f32_e32 v167, 0x41800000, v76
	v_med3_f32 v164, v164, s25, v5
	v_med3_f32 v165, v165, s25, v5
	v_med3_f32 v166, v166, s25, v5
	v_med3_f32 v167, v167, s25, v5
	v_cvt_pk_fp8_f32 v147, v164, v165
	v_cvt_pk_fp8_f32 v147, v166, v167 op_sel:[0,0,1]
	s_nop 0
	global_store_dwordx4 v7, v[144:147], s[20:21] nt
	s_add_u32 s20, s20, s19
	s_addc_u32 s21, s21, 0
	v_mul_f32_e32 v160, 0x41800000, v17
	v_mul_f32_e32 v161, 0x41800000, v21
	v_mul_f32_e32 v162, 0x41800000, v25
	v_mul_f32_e32 v163, 0x41800000, v29
	v_med3_f32 v160, v160, s25, v5
	v_med3_f32 v161, v161, s25, v5
	v_med3_f32 v162, v162, s25, v5
	v_med3_f32 v163, v163, s25, v5
	v_cvt_pk_fp8_f32 v148, v160, v161
	v_cvt_pk_fp8_f32 v148, v162, v163 op_sel:[0,0,1]
	v_mul_f32_e32 v164, 0x41800000, v33
	v_mul_f32_e32 v165, 0x41800000, v37
	v_mul_f32_e32 v166, 0x41800000, v41
	v_mul_f32_e32 v167, 0x41800000, v45
	v_med3_f32 v164, v164, s25, v5
	v_med3_f32 v165, v165, s25, v5
	v_med3_f32 v166, v166, s25, v5
	v_med3_f32 v167, v167, s25, v5
	v_cvt_pk_fp8_f32 v149, v164, v165
	v_cvt_pk_fp8_f32 v149, v166, v167 op_sel:[0,0,1]
	v_mul_f32_e32 v160, 0x41800000, v49
	v_mul_f32_e32 v161, 0x41800000, v53
	v_mul_f32_e32 v162, 0x41800000, v57
	v_mul_f32_e32 v163, 0x41800000, v61
	v_med3_f32 v160, v160, s25, v5
	v_med3_f32 v161, v161, s25, v5
	v_med3_f32 v162, v162, s25, v5
	v_med3_f32 v163, v163, s25, v5
	v_cvt_pk_fp8_f32 v150, v160, v161
	v_cvt_pk_fp8_f32 v150, v162, v163 op_sel:[0,0,1]
	v_mul_f32_e32 v164, 0x41800000, v65
	v_mul_f32_e32 v165, 0x41800000, v69
	v_mul_f32_e32 v166, 0x41800000, v73
	v_mul_f32_e32 v167, 0x41800000, v77
	v_med3_f32 v164, v164, s25, v5
	v_med3_f32 v165, v165, s25, v5
	v_med3_f32 v166, v166, s25, v5
	v_med3_f32 v167, v167, s25, v5
	v_cvt_pk_fp8_f32 v151, v164, v165
	v_cvt_pk_fp8_f32 v151, v166, v167 op_sel:[0,0,1]
	s_nop 0
	global_store_dwordx4 v7, v[148:151], s[20:21] nt
	s_add_u32 s20, s20, s19
	s_addc_u32 s21, s21, 0
	v_mul_f32_e32 v160, 0x41800000, v18
	v_mul_f32_e32 v161, 0x41800000, v22
	v_mul_f32_e32 v162, 0x41800000, v26
	v_mul_f32_e32 v163, 0x41800000, v30
	v_med3_f32 v160, v160, s25, v5
	v_med3_f32 v161, v161, s25, v5
	v_med3_f32 v162, v162, s25, v5
	v_med3_f32 v163, v163, s25, v5
	v_cvt_pk_fp8_f32 v152, v160, v161
	v_cvt_pk_fp8_f32 v152, v162, v163 op_sel:[0,0,1]
	v_mul_f32_e32 v164, 0x41800000, v34
	v_mul_f32_e32 v165, 0x41800000, v38
	v_mul_f32_e32 v166, 0x41800000, v42
	v_mul_f32_e32 v167, 0x41800000, v46
	v_med3_f32 v164, v164, s25, v5
	v_med3_f32 v165, v165, s25, v5
	v_med3_f32 v166, v166, s25, v5
	v_med3_f32 v167, v167, s25, v5
	v_cvt_pk_fp8_f32 v153, v164, v165
	v_cvt_pk_fp8_f32 v153, v166, v167 op_sel:[0,0,1]
	v_mul_f32_e32 v160, 0x41800000, v50
	v_mul_f32_e32 v161, 0x41800000, v54
	v_mul_f32_e32 v162, 0x41800000, v58
	v_mul_f32_e32 v163, 0x41800000, v62
	v_med3_f32 v160, v160, s25, v5
	v_med3_f32 v161, v161, s25, v5
	v_med3_f32 v162, v162, s25, v5
	v_med3_f32 v163, v163, s25, v5
	v_cvt_pk_fp8_f32 v154, v160, v161
	v_cvt_pk_fp8_f32 v154, v162, v163 op_sel:[0,0,1]
	v_mul_f32_e32 v164, 0x41800000, v66
	v_mul_f32_e32 v165, 0x41800000, v70
	v_mul_f32_e32 v166, 0x41800000, v74
	v_mul_f32_e32 v167, 0x41800000, v78
	v_med3_f32 v164, v164, s25, v5
	v_med3_f32 v165, v165, s25, v5
	v_med3_f32 v166, v166, s25, v5
	v_med3_f32 v167, v167, s25, v5
	v_cvt_pk_fp8_f32 v155, v164, v165
	v_cvt_pk_fp8_f32 v155, v166, v167 op_sel:[0,0,1]
	s_nop 0
	global_store_dwordx4 v7, v[152:155], s[20:21] nt
	s_add_u32 s20, s20, s19
	s_addc_u32 s21, s21, 0
	v_mul_f32_e32 v160, 0x41800000, v19
	v_mul_f32_e32 v161, 0x41800000, v23
	v_mul_f32_e32 v162, 0x41800000, v27
	v_mul_f32_e32 v163, 0x41800000, v31
	v_med3_f32 v160, v160, s25, v5
	v_med3_f32 v161, v161, s25, v5
	v_med3_f32 v162, v162, s25, v5
	v_med3_f32 v163, v163, s25, v5
	v_cvt_pk_fp8_f32 v156, v160, v161
	v_cvt_pk_fp8_f32 v156, v162, v163 op_sel:[0,0,1]
	v_mul_f32_e32 v164, 0x41800000, v35
	v_mul_f32_e32 v165, 0x41800000, v39
	v_mul_f32_e32 v166, 0x41800000, v43
	v_mul_f32_e32 v167, 0x41800000, v47
	v_med3_f32 v164, v164, s25, v5
	v_med3_f32 v165, v165, s25, v5
	v_med3_f32 v166, v166, s25, v5
	v_med3_f32 v167, v167, s25, v5
	v_cvt_pk_fp8_f32 v157, v164, v165
	v_cvt_pk_fp8_f32 v157, v166, v167 op_sel:[0,0,1]
	v_mul_f32_e32 v160, 0x41800000, v51
	v_mul_f32_e32 v161, 0x41800000, v55
	v_mul_f32_e32 v162, 0x41800000, v59
	v_mul_f32_e32 v163, 0x41800000, v63
	v_med3_f32 v160, v160, s25, v5
	v_med3_f32 v161, v161, s25, v5
	v_med3_f32 v162, v162, s25, v5
	v_med3_f32 v163, v163, s25, v5
	v_cvt_pk_fp8_f32 v158, v160, v161
	v_cvt_pk_fp8_f32 v158, v162, v163 op_sel:[0,0,1]
	v_mul_f32_e32 v164, 0x41800000, v67
	v_mul_f32_e32 v165, 0x41800000, v71
	v_mul_f32_e32 v166, 0x41800000, v75
	v_mul_f32_e32 v167, 0x41800000, v79
	v_med3_f32 v164, v164, s25, v5
	v_med3_f32 v165, v165, s25, v5
	v_med3_f32 v166, v166, s25, v5
	v_med3_f32 v167, v167, s25, v5
	v_cvt_pk_fp8_f32 v159, v164, v165
	v_cvt_pk_fp8_f32 v159, v166, v167 op_sel:[0,0,1]
	s_nop 0
	global_store_dwordx4 v7, v[156:159], s[20:21] nt
	s_branch .Lconv_done
.Lconv_tailB:
	s_waitcnt vmcnt(0)
	v_mul_f32_e32 v160, 0x41800000, v80
	v_mul_f32_e32 v161, 0x41800000, v84
	v_mul_f32_e32 v162, 0x41800000, v88
	v_mul_f32_e32 v163, 0x41800000, v92
	v_med3_f32 v160, v160, s25, v5
	v_med3_f32 v161, v161, s25, v5
	v_med3_f32 v162, v162, s25, v5
	v_med3_f32 v163, v163, s25, v5
	v_cvt_pk_fp8_f32 v144, v160, v161
	v_cvt_pk_fp8_f32 v144, v162, v163 op_sel:[0,0,1]
	v_mul_f32_e32 v164, 0x41800000, v96
	v_mul_f32_e32 v165, 0x41800000, v100
	v_mul_f32_e32 v166, 0x41800000, v104
	v_mul_f32_e32 v167, 0x41800000, v108
	v_med3_f32 v164, v164, s25, v5
	v_med3_f32 v165, v165, s25, v5
	v_med3_f32 v166, v166, s25, v5
	v_med3_f32 v167, v167, s25, v5
	v_cvt_pk_fp8_f32 v145, v164, v165
	v_cvt_pk_fp8_f32 v145, v166, v167 op_sel:[0,0,1]
	v_mul_f32_e32 v160, 0x41800000, v112
	v_mul_f32_e32 v161, 0x41800000, v116
	v_mul_f32_e32 v162, 0x41800000, v120
	v_mul_f32_e32 v163, 0x41800000, v124
	v_med3_f32 v160, v160, s25, v5
	v_med3_f32 v161, v161, s25, v5
	v_med3_f32 v162, v162, s25, v5
	v_med3_f32 v163, v163, s25, v5
	v_cvt_pk_fp8_f32 v146, v160, v161
	v_cvt_pk_fp8_f32 v146, v162, v163 op_sel:[0,0,1]
	v_mul_f32_e32 v164, 0x41800000, v128
	v_mul_f32_e32 v165, 0x41800000, v132
	v_mul_f32_e32 v166, 0x41800000, v136
	v_mul_f32_e32 v167, 0x41800000, v140
	v_med3_f32 v164, v164, s25, v5
	v_med3_f32 v165, v165, s25, v5
	v_med3_f32 v166, v166, s25, v5
	v_med3_f32 v167, v167, s25, v5
	v_cvt_pk_fp8_f32 v147, v164, v165
	v_cvt_pk_fp8_f32 v147, v166, v167 op_sel:[0,0,1]
	s_nop 0
	global_store_dwordx4 v8, v[144:147], s[22:23] nt
	s_add_u32 s22, s22, s24
	s_addc_u32 s23, s23, 0
	v_mul_f32_e32 v160, 0x41800000, v81
	v_mul_f32_e32 v161, 0x41800000, v85
	v_mul_f32_e32 v162, 0x41800000, v89
	v_mul_f32_e32 v163, 0x41800000, v93
	v_med3_f32 v160, v160, s25, v5
	v_med3_f32 v161, v161, s25, v5
	v_med3_f32 v162, v162, s25, v5
	v_med3_f32 v163, v163, s25, v5
	v_cvt_pk_fp8_f32 v148, v160, v161
	v_cvt_pk_fp8_f32 v148, v162, v163 op_sel:[0,0,1]
	v_mul_f32_e32 v164, 0x41800000, v97
	v_mul_f32_e32 v165, 0x41800000, v101
	v_mul_f32_e32 v166, 0x41800000, v105
	v_mul_f32_e32 v167, 0x41800000, v109
	v_med3_f32 v164, v164, s25, v5
	v_med3_f32 v165, v165, s25, v5
	v_med3_f32 v166, v166, s25, v5
	v_med3_f32 v167, v167, s25, v5
	v_cvt_pk_fp8_f32 v149, v164, v165
	v_cvt_pk_fp8_f32 v149, v166, v167 op_sel:[0,0,1]
	v_mul_f32_e32 v160, 0x41800000, v113
	v_mul_f32_e32 v161, 0x41800000, v117
	v_mul_f32_e32 v162, 0x41800000, v121
	v_mul_f32_e32 v163, 0x41800000, v125
	v_med3_f32 v160, v160, s25, v5
	v_med3_f32 v161, v161, s25, v5
	v_med3_f32 v162, v162, s25, v5
	v_med3_f32 v163, v163, s25, v5
	v_cvt_pk_fp8_f32 v150, v160, v161
	v_cvt_pk_fp8_f32 v150, v162, v163 op_sel:[0,0,1]
	v_mul_f32_e32 v164, 0x41800000, v129
	v_mul_f32_e32 v165, 0x41800000, v133
	v_mul_f32_e32 v166, 0x41800000, v137
	v_mul_f32_e32 v167, 0x41800000, v141
	v_med3_f32 v164, v164, s25, v5
	v_med3_f32 v165, v165, s25, v5
	v_med3_f32 v166, v166, s25, v5
	v_med3_f32 v167, v167, s25, v5
	v_cvt_pk_fp8_f32 v151, v164, v165
	v_cvt_pk_fp8_f32 v151, v166, v167 op_sel:[0,0,1]
	s_nop 0
	global_store_dwordx4 v8, v[148:151], s[22:23] nt
	s_add_u32 s22, s22, s24
	s_addc_u32 s23, s23, 0
	v_mul_f32_e32 v160, 0x41800000, v82
	v_mul_f32_e32 v161, 0x41800000, v86
	v_mul_f32_e32 v162, 0x41800000, v90
	v_mul_f32_e32 v163, 0x41800000, v94
	v_med3_f32 v160, v160, s25, v5
	v_med3_f32 v161, v161, s25, v5
	v_med3_f32 v162, v162, s25, v5
	v_med3_f32 v163, v163, s25, v5
	v_cvt_pk_fp8_f32 v152, v160, v161
	v_cvt_pk_fp8_f32 v152, v162, v163 op_sel:[0,0,1]
	v_mul_f32_e32 v164, 0x41800000, v98
	v_mul_f32_e32 v165, 0x41800000, v102
	v_mul_f32_e32 v166, 0x41800000, v106
	v_mul_f32_e32 v167, 0x41800000, v110
	v_med3_f32 v164, v164, s25, v5
	v_med3_f32 v165, v165, s25, v5
	v_med3_f32 v166, v166, s25, v5
	v_med3_f32 v167, v167, s25, v5
	v_cvt_pk_fp8_f32 v153, v164, v165
	v_cvt_pk_fp8_f32 v153, v166, v167 op_sel:[0,0,1]
	v_mul_f32_e32 v160, 0x41800000, v114
	v_mul_f32_e32 v161, 0x41800000, v118
	v_mul_f32_e32 v162, 0x41800000, v122
	v_mul_f32_e32 v163, 0x41800000, v126
	v_med3_f32 v160, v160, s25, v5
	v_med3_f32 v161, v161, s25, v5
	v_med3_f32 v162, v162, s25, v5
	v_med3_f32 v163, v163, s25, v5
	v_cvt_pk_fp8_f32 v154, v160, v161
	v_cvt_pk_fp8_f32 v154, v162, v163 op_sel:[0,0,1]
	v_mul_f32_e32 v164, 0x41800000, v130
	v_mul_f32_e32 v165, 0x41800000, v134
	v_mul_f32_e32 v166, 0x41800000, v138
	v_mul_f32_e32 v167, 0x41800000, v142
	v_med3_f32 v164, v164, s25, v5
	v_med3_f32 v165, v165, s25, v5
	v_med3_f32 v166, v166, s25, v5
	v_med3_f32 v167, v167, s25, v5
	v_cvt_pk_fp8_f32 v155, v164, v165
	v_cvt_pk_fp8_f32 v155, v166, v167 op_sel:[0,0,1]
	s_nop 0
	global_store_dwordx4 v8, v[152:155], s[22:23] nt
	s_add_u32 s22, s22, s24
	s_addc_u32 s23, s23, 0
	v_mul_f32_e32 v160, 0x41800000, v83
	v_mul_f32_e32 v161, 0x41800000, v87
	v_mul_f32_e32 v162, 0x41800000, v91
	v_mul_f32_e32 v163, 0x41800000, v95
	v_med3_f32 v160, v160, s25, v5
	v_med3_f32 v161, v161, s25, v5
	v_med3_f32 v162, v162, s25, v5
	v_med3_f32 v163, v163, s25, v5
	v_cvt_pk_fp8_f32 v156, v160, v161
	v_cvt_pk_fp8_f32 v156, v162, v163 op_sel:[0,0,1]
	v_mul_f32_e32 v164, 0x41800000, v99
	v_mul_f32_e32 v165, 0x41800000, v103
	v_mul_f32_e32 v166, 0x41800000, v107
	v_mul_f32_e32 v167, 0x41800000, v111
	v_med3_f32 v164, v164, s25, v5
	v_med3_f32 v165, v165, s25, v5
	v_med3_f32 v166, v166, s25, v5
	v_med3_f32 v167, v167, s25, v5
	v_cvt_pk_fp8_f32 v157, v164, v165
	v_cvt_pk_fp8_f32 v157, v166, v167 op_sel:[0,0,1]
	v_mul_f32_e32 v160, 0x41800000, v115
	v_mul_f32_e32 v161, 0x41800000, v119
	v_mul_f32_e32 v162, 0x41800000, v123
	v_mul_f32_e32 v163, 0x41800000, v127
	v_med3_f32 v160, v160, s25, v5
	v_med3_f32 v161, v161, s25, v5
	v_med3_f32 v162, v162, s25, v5
	v_med3_f32 v163, v163, s25, v5
	v_cvt_pk_fp8_f32 v158, v160, v161
	v_cvt_pk_fp8_f32 v158, v162, v163 op_sel:[0,0,1]
	v_mul_f32_e32 v164, 0x41800000, v131
	v_mul_f32_e32 v165, 0x41800000, v135
	v_mul_f32_e32 v166, 0x41800000, v139
	v_mul_f32_e32 v167, 0x41800000, v143
	v_med3_f32 v164, v164, s25, v5
	v_med3_f32 v165, v165, s25, v5
	v_med3_f32 v166, v166, s25, v5
	v_med3_f32 v167, v167, s25, v5
	v_cvt_pk_fp8_f32 v159, v164, v165
	v_cvt_pk_fp8_f32 v159, v166, v167 op_sel:[0,0,1]
	s_nop 0
	global_store_dwordx4 v8, v[156:159], s[22:23] nt
.Lconv_done:
	s_cmp_eq_u32 s72, 0
	s_cbranch_scc1 .LBB0_1135
	s_cmp_eq_u32 s72, 1
	s_cbranch_scc1 .LBB0_1178
	s_cmp_eq_u32 s72, 2
	s_cbranch_scc1 .LBB0_1239
	s_branch .LBB0_1515

.LBB0_1157:
	v_exp_f32_e32 v100, v82
	v_exp_f32_e32 v101, v83
	v_exp_f32_e32 v82, v84
	v_fmamk_f32 v66, v66, 0x3e0293ee, v99
	v_exp_f32_e32 v84, v85
	v_fmamk_f32 v113, v77, 0x3e0293ee, v99
	v_exp_f32_e32 v77, v86
	v_exp_f32_e32 v1, v66
	v_add_f32_e32 v66, 0, v100
	v_exp_f32_e32 v83, v87
	v_add_f32_e32 v66, v101, v66
	v_fmamk_f32 v112, v76, 0x3e0293ee, v99
	v_exp_f32_e32 v76, v88
	v_add_f32_e32 v66, v82, v66
	v_fmamk_f32 v114, v78, 0x3e0293ee, v99
	v_exp_f32_e32 v78, v89
	v_add_f32_e32 v66, v84, v66
	v_fmamk_f32 v107, v73, 0x3e0293ee, v99
	v_exp_f32_e32 v73, v90
	v_add_f32_e32 v66, v77, v66
	v_fmamk_f32 v109, v75, 0x3e0293ee, v99
	v_exp_f32_e32 v75, v91
	v_add_f32_e32 v66, v83, v66
	v_fmamk_f32 v105, v71, 0x3e0293ee, v99
	v_exp_f32_e32 v71, v92
	v_add_f32_e32 v66, v76, v66
	v_fmamk_f32 v108, v74, 0x3e0293ee, v99
	v_exp_f32_e32 v74, v93
	v_add_f32_e32 v66, v78, v66
	v_fmamk_f32 v103, v69, 0x3e0293ee, v99
	v_exp_f32_e32 v69, v94
	v_add_f32_e32 v66, v73, v66
	v_fmamk_f32 v106, v72, 0x3e0293ee, v99
	v_exp_f32_e32 v72, v95
	v_add_f32_e32 v66, v75, v66
	v_fmamk_f32 v102, v68, 0x3e0293ee, v99
	v_exp_f32_e32 v68, v96
	v_add_f32_e32 v66, v71, v66
	v_fmamk_f32 v104, v70, 0x3e0293ee, v99
	v_exp_f32_e32 v70, v97
	v_add_f32_e32 v66, v74, v66
	v_fmamk_f32 v67, v67, 0x3e0293ee, v99
	v_add_f32_e32 v66, v69, v66
	v_exp_f32_e32 v85, v67
	v_add_f32_e32 v66, v72, v66
	v_exp_f32_e32 v86, v102
	v_add_f32_e32 v66, v68, v66
	v_exp_f32_e32 v87, v103
	v_add_f32_e32 v66, v70, v66
	v_exp_f32_e32 v88, v104
	v_add_f32_e32 v66, v1, v66
	v_exp_f32_e32 v89, v105
	v_add_f32_e32 v66, v85, v66
	v_exp_f32_e32 v90, v106
	v_add_f32_e32 v66, v86, v66
	v_exp_f32_e32 v91, v107
	v_add_f32_e32 v66, v87, v66
	v_exp_f32_e32 v92, v108
	v_add_f32_e32 v66, v88, v66
	v_exp_f32_e32 v93, v109
	v_add_f32_e32 v66, v89, v66
	v_exp_f32_e32 v94, v112
	v_add_f32_e32 v66, v90, v66
	v_exp_f32_e32 v95, v113
	v_add_f32_e32 v66, v91, v66
	v_fmamk_f32 v79, v79, 0x3e0293ee, v99
	v_exp_f32_e32 v96, v114
	v_add_f32_e32 v66, v92, v66
	v_fmamk_f32 v80, v80, 0x3e0293ee, v99
	v_exp_f32_e32 v97, v79
	v_add_f32_e32 v66, v93, v66
	v_fmac_f32_e32 v99, 0x3e0293ee, v81
	v_exp_f32_e32 v102, v80
	v_add_f32_e32 v66, v94, v66
	v_exp_f32_e32 v99, v99
	v_add_f32_e32 v66, v95, v66
	v_add_f32_e32 v66, v96, v66
	v_add_f32_e32 v66, v97, v66
	v_add_f32_e32 v66, v102, v66
	v_add_f32_e32 v66, v99, v66
	v_mov_b32_e32 v67, v66
	s_nop 1
	v_permlane32_swap_b32_e32 v66, v67
	v_cvt_pk_bf16_f32 v80, v100, v101
	v_cvt_pk_bf16_f32 v81, v82, v84
	v_cvt_pk_bf16_f32 v82, v77, v83
	v_cvt_pk_bf16_f32 v83, v76, v78
	v_cvt_pk_bf16_f32 v76, v73, v75
	v_cvt_pk_bf16_f32 v77, v71, v74
	v_cvt_pk_bf16_f32 v78, v69, v72
	v_cvt_pk_bf16_f32 v79, v68, v70
	v_cvt_pk_bf16_f32 v68, v1, v85
	v_cvt_pk_bf16_f32 v69, v86, v87
	v_cvt_pk_bf16_f32 v70, v88, v89
	v_cvt_pk_bf16_f32 v71, v90, v91
	v_cvt_pk_bf16_f32 v72, v92, v93
	v_cvt_pk_bf16_f32 v73, v94, v95
	v_cvt_pk_bf16_f32 v74, v96, v97
	v_cvt_pk_bf16_f32 v75, v102, v99
	s_nop 0
	v_permlane32_swap_b32_e32 v80, v82
	v_permlane32_swap_b32_e32 v81, v83
	v_permlane32_swap_b32_e32 v76, v78
	v_permlane32_swap_b32_e32 v77, v79
	v_permlane32_swap_b32_e32 v68, v70
	v_permlane32_swap_b32_e32 v69, v71
	v_permlane32_swap_b32_e32 v72, v74
	v_permlane32_swap_b32_e32 v73, v75
	ds_read_b64_tr_b16 v[84:85], v198 offset:0
	ds_read_b64_tr_b16 v[86:87], v198 offset:0x800
	ds_read_b64_tr_b16 v[88:89], v198 offset:0x1000
	ds_read_b64_tr_b16 v[90:91], v198 offset:0x1800
	ds_read_b64_tr_b16 v[92:93], v198 offset:0x2000
	ds_read_b64_tr_b16 v[94:95], v198 offset:0x2800
	ds_read_b64_tr_b16 v[100:101], v198 offset:0x3000
	ds_read_b64_tr_b16 v[102:103], v198 offset:0x3800
	s_waitcnt lgkmcnt(0)
	s_nop 0
	v_mfma_f32_32x32x16_bf16 v[18:33], v[80:83], v[84:87], v[18:33]
	ds_read_b64_tr_b16 v[84:85], v198 offset:0x200
	ds_read_b64_tr_b16 v[86:87], v198 offset:0xa00
	v_mfma_f32_32x32x16_bf16 v[18:33], v[76:79], v[88:91], v[18:33]
	ds_read_b64_tr_b16 v[88:89], v198 offset:0x1200
	ds_read_b64_tr_b16 v[90:91], v198 offset:0x1a00
	v_mfma_f32_32x32x16_bf16 v[18:33], v[68:71], v[92:95], v[18:33]
	ds_read_b64_tr_b16 v[92:93], v198 offset:0x2200
	ds_read_b64_tr_b16 v[94:95], v198 offset:0x2a00
	ds_read_b64_tr_b16 v[104:105], v198 offset:0x3200
	ds_read_b64_tr_b16 v[106:107], v198 offset:0x3a00
	s_waitcnt lgkmcnt(0)
	v_mfma_f32_32x32x16_bf16 v[18:33], v[72:75], v[100:103], v[18:33]
	v_mfma_f32_32x32x16_bf16 v[50:65], v[80:83], v[84:87], v[50:65]
	ds_read_b64_tr_b16 v[84:85], v198 offset:0x400
	ds_read_b64_tr_b16 v[86:87], v198 offset:0xc00
	v_mfma_f32_32x32x16_bf16 v[50:65], v[76:79], v[88:91], v[50:65]
	ds_read_b64_tr_b16 v[88:89], v198 offset:0x1400
	ds_read_b64_tr_b16 v[90:91], v198 offset:0x1c00
	v_mfma_f32_32x32x16_bf16 v[50:65], v[68:71], v[92:95], v[50:65]
	ds_read_b64_tr_b16 v[92:93], v198 offset:0x2400
	ds_read_b64_tr_b16 v[94:95], v198 offset:0x2c00
	ds_read_b64_tr_b16 v[100:101], v198 offset:0x3400
	ds_read_b64_tr_b16 v[102:103], v198 offset:0x3c00
	s_waitcnt lgkmcnt(0)
	v_mfma_f32_32x32x16_bf16 v[50:65], v[72:75], v[104:107], v[50:65]
	v_mfma_f32_32x32x16_bf16 v[34:49], v[80:83], v[84:87], v[34:49]
	ds_read_b64_tr_b16 v[84:85], v198 offset:0x600
	ds_read_b64_tr_b16 v[86:87], v198 offset:0xe00
	v_mfma_f32_32x32x16_bf16 v[34:49], v[76:79], v[88:91], v[34:49]
	ds_read_b64_tr_b16 v[88:89], v198 offset:0x1600
	ds_read_b64_tr_b16 v[90:91], v198 offset:0x1e00
	v_mfma_f32_32x32x16_bf16 v[34:49], v[68:71], v[92:95], v[34:49]
	ds_read_b64_tr_b16 v[92:93], v198 offset:0x2600
	ds_read_b64_tr_b16 v[94:95], v198 offset:0x2e00
	ds_read_b64_tr_b16 v[104:105], v198 offset:0x3600
	ds_read_b64_tr_b16 v[106:107], v198 offset:0x3e00
	s_waitcnt lgkmcnt(0)
	v_mfma_f32_32x32x16_bf16 v[34:49], v[72:75], v[100:103], v[34:49]
	v_mfma_f32_32x32x16_bf16 v[2:17], v[80:83], v[84:87], v[2:17]
	v_mfma_f32_32x32x16_bf16 v[2:17], v[76:79], v[88:91], v[2:17]
	v_mfma_f32_32x32x16_bf16 v[2:17], v[68:71], v[92:95], v[2:17]
	v_mfma_f32_32x32x16_bf16 v[2:17], v[72:75], v[104:107], v[2:17]
	s_and_saveexec_b64 s[2:3], s[0:1]
	v_add_f32_e32 v1, v110, v111
	v_fmac_f32_e32 v1, v183, v162
	v_add_f32_e32 v66, v66, v67
	v_fmac_f32_e32 v66, v1, v98
	ds_write_b32 v197, v66
	s_or_b64 exec, exec, s[2:3]
	s_waitcnt lgkmcnt(0)
	v_add_u32_e32 v1, v196, v182
	ds_read_b128 v[66:69], v1
	ds_read_b128 v[70:73], v1 offset:32
	s_add_u32 s0, s4, s10
	s_addc_u32 s1, s5, s11
	s_add_i32 s2, 0, 0x10800
	s_waitcnt lgkmcnt(1)
	v_rcp_f32_e32 v74, v66
	v_rcp_f32_e32 v75, v67
	v_rcp_f32_e32 v76, v68
	v_rcp_f32_e32 v77, v69
	s_waitcnt lgkmcnt(0)
	v_rcp_f32_e32 v78, v70
	ds_read_b128 v[66:69], v1 offset:64
	v_rcp_f32_e32 v79, v71
	v_rcp_f32_e32 v80, v72
	v_rcp_f32_e32 v81, v73
	ds_read_b128 v[70:73], v1 offset:96
	s_waitcnt lgkmcnt(1)
	v_rcp_f32_e32 v1, v66
	v_rcp_f32_e32 v66, v67
	v_rcp_f32_e32 v67, v68
	v_rcp_f32_e32 v68, v69
	s_waitcnt lgkmcnt(0)
	v_rcp_f32_e32 v69, v70
	v_rcp_f32_e32 v70, v71
	v_rcp_f32_e32 v71, v72
	v_rcp_f32_e32 v72, v73
	v_lshl_add_u32 v73, v181, 13, s2
	v_mul_f32_e32 v18, v18, v74
	s_mov_b32 s2, 0xc3e00000
	v_mov_b32_e32 v83, 0x43e00000
	v_mul_f32_e32 v19, v19, v75
	v_med3_f32 v18, v18, s2, v83
	v_med3_f32 v19, v19, s2, v83
	v_mov_b32_e32 v84, 0
	v_cvt_pk_fp8_f32 v84, v18, v19
	v_mul_f32_e32 v18, v20, v76
	v_mul_f32_e32 v19, v21, v77
	v_med3_f32 v18, v18, s2, v83
	v_med3_f32 v19, v19, s2, v83
	v_mov_b32_e32 v20, 0
	v_cvt_pk_fp8_f32 v20, v18, v19
	v_lshlrev_b32_e32 v82, 9, v193
	v_add3_u32 v82, v73, v82, v179
	v_lshrrev_b32_e32 v18, 8, v84
	ds_write_b8 v82, v84
	ds_write_b8 v82, v18 offset:128
	ds_write_b8 v82, v20 offset:256
	v_lshrrev_b32_e32 v18, 8, v20
	ds_write_b8 v82, v18 offset:384
	v_mul_f32_e32 v18, v22, v78
	v_mul_f32_e32 v19, v23, v79
	v_med3_f32 v18, v18, s2, v83
	v_med3_f32 v19, v19, s2, v83
	v_mov_b32_e32 v20, 0
	v_cvt_pk_fp8_f32 v20, v18, v19
	v_mul_f32_e32 v18, v24, v80
	v_mul_f32_e32 v19, v25, v81
	v_med3_f32 v18, v18, s2, v83
	v_med3_f32 v19, v19, s2, v83
	v_mov_b32_e32 v21, 0
	v_cvt_pk_fp8_f32 v21, v18, v19
	v_lshrrev_b32_e32 v18, 8, v20
	ds_write_b8 v82, v20 offset:1024
	ds_write_b8 v82, v18 offset:1152
	ds_write_b8 v82, v21 offset:1280
	v_lshrrev_b32_e32 v18, 8, v21
	ds_write_b8 v82, v18 offset:1408
	v_mul_f32_e32 v18, v26, v1
	v_mul_f32_e32 v19, v27, v66
	v_med3_f32 v18, v18, s2, v83
	v_med3_f32 v19, v19, s2, v83
	v_mov_b32_e32 v20, 0
	v_cvt_pk_fp8_f32 v20, v18, v19
	v_mul_f32_e32 v18, v28, v67
	v_mul_f32_e32 v19, v29, v68
	v_med3_f32 v18, v18, s2, v83
	v_med3_f32 v19, v19, s2, v83
	v_mov_b32_e32 v21, 0
	v_cvt_pk_fp8_f32 v21, v18, v19
	v_lshrrev_b32_e32 v18, 8, v20
	ds_write_b8 v82, v20 offset:2048
	ds_write_b8 v82, v18 offset:2176
	ds_write_b8 v82, v21 offset:2304
	v_lshrrev_b32_e32 v18, 8, v21
	ds_write_b8 v82, v18 offset:2432
	v_mul_f32_e32 v18, v30, v69
	v_mul_f32_e32 v19, v31, v70
	v_med3_f32 v18, v18, s2, v83
	v_med3_f32 v19, v19, s2, v83
	v_mov_b32_e32 v20, 0
	v_cvt_pk_fp8_f32 v20, v18, v19
	v_mul_f32_e32 v18, v32, v71
	v_mul_f32_e32 v19, v33, v72
	v_med3_f32 v18, v18, s2, v83
	v_med3_f32 v19, v19, s2, v83
	v_mov_b32_e32 v21, 0
	v_cvt_pk_fp8_f32 v21, v18, v19
	v_lshrrev_b32_e32 v18, 8, v20
	ds_write_b8 v82, v20 offset:3072
	ds_write_b8 v82, v18 offset:3200
	ds_write_b8 v82, v21 offset:3328
	v_lshrrev_b32_e32 v18, 8, v21
	ds_write_b8 v82, v18 offset:3456
	v_mul_f32_e32 v18, v50, v74
	v_mul_f32_e32 v19, v51, v75
	v_med3_f32 v18, v18, s2, v83
	v_med3_f32 v19, v19, s2, v83
	v_mov_b32_e32 v20, 0
	v_cvt_pk_fp8_f32 v20, v18, v19
	v_mul_f32_e32 v18, v52, v76
	v_mul_f32_e32 v19, v53, v77
	v_med3_f32 v18, v18, s2, v83
	v_med3_f32 v19, v19, s2, v83
	v_mov_b32_e32 v21, 0
	v_cvt_pk_fp8_f32 v21, v18, v19
	v_lshrrev_b32_e32 v18, 8, v20
	ds_write_b8 v82, v20 offset:32
	ds_write_b8 v82, v18 offset:160
	ds_write_b8 v82, v21 offset:288
	v_lshrrev_b32_e32 v18, 8, v21
	ds_write_b8 v82, v18 offset:416
	v_mul_f32_e32 v18, v54, v78
	v_mul_f32_e32 v19, v55, v79
	v_med3_f32 v18, v18, s2, v83
	v_med3_f32 v19, v19, s2, v83
	v_mov_b32_e32 v20, 0
	v_cvt_pk_fp8_f32 v20, v18, v19
	v_mul_f32_e32 v18, v56, v80
	v_mul_f32_e32 v19, v57, v81
	v_med3_f32 v18, v18, s2, v83
	v_med3_f32 v19, v19, s2, v83
	v_mov_b32_e32 v21, 0
	v_cvt_pk_fp8_f32 v21, v18, v19
	v_lshrrev_b32_e32 v18, 8, v20
	ds_write_b8 v82, v20 offset:1056
	ds_write_b8 v82, v18 offset:1184
	ds_write_b8 v82, v21 offset:1312
	v_lshrrev_b32_e32 v18, 8, v21
	ds_write_b8 v82, v18 offset:1440
	v_mul_f32_e32 v18, v58, v1
	v_mul_f32_e32 v19, v59, v66
	v_med3_f32 v18, v18, s2, v83
	v_med3_f32 v19, v19, s2, v83
	v_mov_b32_e32 v20, 0
	v_cvt_pk_fp8_f32 v20, v18, v19
	v_mul_f32_e32 v18, v60, v67
	v_mul_f32_e32 v19, v61, v68
	v_med3_f32 v18, v18, s2, v83
	v_med3_f32 v19, v19, s2, v83
	v_mov_b32_e32 v21, 0
	v_cvt_pk_fp8_f32 v21, v18, v19
	v_lshrrev_b32_e32 v18, 8, v20
	ds_write_b8 v82, v20 offset:2080
	ds_write_b8 v82, v18 offset:2208
	ds_write_b8 v82, v21 offset:2336
	v_lshrrev_b32_e32 v18, 8, v21
	ds_write_b8 v82, v18 offset:2464
	v_mul_f32_e32 v18, v62, v69
	v_mul_f32_e32 v19, v63, v70
	v_med3_f32 v18, v18, s2, v83
	v_med3_f32 v19, v19, s2, v83
	v_mov_b32_e32 v20, 0
	v_cvt_pk_fp8_f32 v20, v18, v19
	v_mul_f32_e32 v18, v64, v71
	v_mul_f32_e32 v19, v65, v72
	v_med3_f32 v18, v18, s2, v83
	v_med3_f32 v19, v19, s2, v83
	v_mov_b32_e32 v21, 0
	v_cvt_pk_fp8_f32 v21, v18, v19
	v_lshrrev_b32_e32 v18, 8, v20
	ds_write_b8 v82, v20 offset:3104
	ds_write_b8 v82, v18 offset:3232
	ds_write_b8 v82, v21 offset:3360
	v_lshrrev_b32_e32 v18, 8, v21
	ds_write_b8 v82, v18 offset:3488
	v_mul_f32_e32 v18, v34, v74
	v_mul_f32_e32 v19, v35, v75
	v_med3_f32 v18, v18, s2, v83
	v_med3_f32 v19, v19, s2, v83
	v_mov_b32_e32 v20, 0
	v_cvt_pk_fp8_f32 v20, v18, v19
	v_mul_f32_e32 v18, v36, v76
	v_mul_f32_e32 v19, v37, v77
	v_med3_f32 v18, v18, s2, v83
	v_med3_f32 v19, v19, s2, v83
	v_mov_b32_e32 v21, 0
	v_cvt_pk_fp8_f32 v21, v18, v19
	v_lshrrev_b32_e32 v18, 8, v20
	ds_write_b8 v82, v20 offset:64
	ds_write_b8 v82, v18 offset:192
	ds_write_b8 v82, v21 offset:320
	v_lshrrev_b32_e32 v18, 8, v21
	ds_write_b8 v82, v18 offset:448
	v_mul_f32_e32 v18, v38, v78
	v_mul_f32_e32 v19, v39, v79
	v_med3_f32 v18, v18, s2, v83
	v_med3_f32 v19, v19, s2, v83
	v_mov_b32_e32 v20, 0
	v_cvt_pk_fp8_f32 v20, v18, v19
	v_mul_f32_e32 v18, v40, v80
	v_mul_f32_e32 v19, v41, v81
	v_med3_f32 v18, v18, s2, v83
	v_med3_f32 v19, v19, s2, v83
	v_mov_b32_e32 v21, 0
	v_cvt_pk_fp8_f32 v21, v18, v19
	v_lshrrev_b32_e32 v18, 8, v20
	ds_write_b8 v82, v20 offset:1088
	ds_write_b8 v82, v18 offset:1216
	ds_write_b8 v82, v21 offset:1344
	v_lshrrev_b32_e32 v18, 8, v21
	ds_write_b8 v82, v18 offset:1472
	v_mul_f32_e32 v18, v42, v1
	v_mul_f32_e32 v19, v43, v66
	v_med3_f32 v18, v18, s2, v83
	v_med3_f32 v19, v19, s2, v83
	v_mov_b32_e32 v20, 0
	v_cvt_pk_fp8_f32 v20, v18, v19
	v_mul_f32_e32 v18, v44, v67
	v_mul_f32_e32 v19, v45, v68
	v_med3_f32 v18, v18, s2, v83
	v_med3_f32 v19, v19, s2, v83
	v_mov_b32_e32 v21, 0
	v_cvt_pk_fp8_f32 v21, v18, v19
	v_lshrrev_b32_e32 v18, 8, v20
	ds_write_b8 v82, v20 offset:2112
	ds_write_b8 v82, v18 offset:2240
	ds_write_b8 v82, v21 offset:2368
	v_lshrrev_b32_e32 v18, 8, v21
	ds_write_b8 v82, v18 offset:2496
	v_mul_f32_e32 v18, v46, v69
	v_mul_f32_e32 v19, v47, v70
	v_med3_f32 v18, v18, s2, v83
	v_med3_f32 v19, v19, s2, v83
	v_mov_b32_e32 v20, 0
	v_cvt_pk_fp8_f32 v20, v18, v19
	v_mul_f32_e32 v18, v48, v71
	v_mul_f32_e32 v19, v49, v72
	v_med3_f32 v18, v18, s2, v83
	v_med3_f32 v19, v19, s2, v83
	v_mov_b32_e32 v21, 0
	v_cvt_pk_fp8_f32 v21, v18, v19
	v_lshrrev_b32_e32 v18, 8, v20
	ds_write_b8 v82, v20 offset:3136
	ds_write_b8 v82, v18 offset:3264
	ds_write_b8 v82, v21 offset:3392
	v_lshrrev_b32_e32 v18, 8, v21
	v_mul_f32_e32 v2, v2, v74
	v_mul_f32_e32 v3, v3, v75
	ds_write_b8 v82, v18 offset:3520
	v_med3_f32 v2, v2, s2, v83
	v_med3_f32 v3, v3, s2, v83
	v_mov_b32_e32 v18, 0
	v_cvt_pk_fp8_f32 v18, v2, v3
	v_mul_f32_e32 v2, v4, v76
	v_mul_f32_e32 v3, v5, v77
	v_med3_f32 v2, v2, s2, v83
	v_med3_f32 v3, v3, s2, v83
	v_mov_b32_e32 v4, 0
	v_cvt_pk_fp8_f32 v4, v2, v3
	v_lshrrev_b32_e32 v2, 8, v18
	ds_write_b8 v82, v18 offset:96
	ds_write_b8 v82, v2 offset:224
	ds_write_b8 v82, v4 offset:352
	v_lshrrev_b32_e32 v2, 8, v4
	ds_write_b8 v82, v2 offset:480
	v_mul_f32_e32 v2, v6, v78
	v_mul_f32_e32 v3, v7, v79
	v_med3_f32 v2, v2, s2, v83
	v_med3_f32 v3, v3, s2, v83
	v_mov_b32_e32 v4, 0
	v_cvt_pk_fp8_f32 v4, v2, v3
	v_mul_f32_e32 v2, v8, v80
	v_mul_f32_e32 v3, v9, v81
	v_med3_f32 v2, v2, s2, v83
	v_med3_f32 v3, v3, s2, v83
	v_mov_b32_e32 v5, 0
	v_cvt_pk_fp8_f32 v5, v2, v3
	v_lshrrev_b32_e32 v2, 8, v4
	ds_write_b8 v82, v4 offset:1120
	ds_write_b8 v82, v2 offset:1248
	ds_write_b8 v82, v5 offset:1376
	v_lshrrev_b32_e32 v2, 8, v5
	ds_write_b8 v82, v2 offset:1504
	v_mul_f32_e32 v1, v10, v1
	v_mul_f32_e32 v2, v11, v66
	v_med3_f32 v1, v1, s2, v83
	v_med3_f32 v2, v2, s2, v83
	v_mov_b32_e32 v3, 0
	v_cvt_pk_fp8_f32 v3, v1, v2
	v_mul_f32_e32 v1, v12, v67
	v_mul_f32_e32 v2, v13, v68
	v_med3_f32 v1, v1, s2, v83
	v_med3_f32 v2, v2, s2, v83
	v_mov_b32_e32 v4, 0
	v_cvt_pk_fp8_f32 v4, v1, v2
	v_lshrrev_b32_e32 v1, 8, v3
	ds_write_b8 v82, v3 offset:2144
	ds_write_b8 v82, v1 offset:2272
	ds_write_b8 v82, v4 offset:2400
	v_lshrrev_b32_e32 v1, 8, v4
	ds_write_b8 v82, v1 offset:2528
	v_mul_f32_e32 v1, v14, v69
	v_mul_f32_e32 v2, v15, v70
	v_med3_f32 v1, v1, s2, v83
	v_med3_f32 v2, v2, s2, v83
	v_mov_b32_e32 v3, 0
	v_cvt_pk_fp8_f32 v3, v1, v2
	v_mul_f32_e32 v1, v16, v71
	v_mul_f32_e32 v2, v17, v72
	v_med3_f32 v1, v1, s2, v83
	v_med3_f32 v2, v2, s2, v83
	v_mov_b32_e32 v4, 0
	v_cvt_pk_fp8_f32 v4, v1, v2
	v_lshrrev_b32_e32 v1, 8, v3
	ds_write_b8 v82, v3 offset:3168
	ds_write_b8 v82, v1 offset:3296
	ds_write_b8 v82, v4 offset:3424
	v_lshrrev_b32_e32 v1, 8, v4
	ds_write_b8 v82, v1 offset:3552
	v_lshrrev_b32_e32 v1, 3, v254
	v_lshlrev_b32_e32 v2, 7, v1
	v_mov_b32_e32 v181, 0
	s_waitcnt lgkmcnt(0)
	v_add3_u32 v14, v73, v2, v178
	v_lshl_add_u64 v[6:7], s[0:1], 0, v[180:181]
	v_lshlrev_b32_e32 v180, 11, v1
	ds_read_b128 v[2:5], v14
	v_lshl_add_u64 v[6:7], v[6:7], 0, v[180:181]
	v_mov_b32_e32 v179, v181
	v_lshl_add_u64 v[10:11], v[6:7], 0, v[178:179]
	ds_read_b128 v[6:9], v14 offset:1024
	s_movk_i32 s0, 0x4000
	s_waitcnt lgkmcnt(1)
	global_store_dwordx4 v[10:11], v[2:5], off
	s_nop 1
	v_add_co_u32_e32 v2, vcc, s0, v10
	s_nop 1
	v_addc_co_u32_e32 v3, vcc, 0, v11, vcc
	s_waitcnt lgkmcnt(0)
	global_store_dwordx4 v[2:3], v[6:9], off
	ds_read_b128 v[2:5], v14 offset:2048
	ds_read_b128 v[6:9], v14 offset:3072
	v_add_co_u32_e32 v12, vcc, 0x8000, v10
	s_nop 1
	v_addc_co_u32_e32 v13, vcc, 0, v11, vcc
	s_waitcnt lgkmcnt(1)
	global_store_dwordx4 v[12:13], v[2:5], off
	s_nop 1
	v_add_co_u32_e32 v2, vcc, 0xc000, v10
	s_nop 1
	v_addc_co_u32_e32 v3, vcc, 0, v11, vcc
	s_waitcnt lgkmcnt(0)
	global_store_dwordx4 v[2:3], v[6:9], off
	s_waitcnt lgkmcnt(0)
	s_barrier
	s_cmp_lg_u32 s72, 1
	s_cbranch_scc1 .LBB0_1138
.LBB0_1160:
	s_branch .Lconv_entry
.LBB0_1178:
	s_waitcnt lgkmcnt(0)
	s_barrier
	s_add_i32 s0, s76, s33
	s_cmpk_gt_i32 s0, 0x1ff
	s_cbranch_scc1 .LBB0_1139

.LBB0_1220:
	s_cmp_eq_u32 s72, 2
	s_cbranch_scc0 .LBB0_1240
	s_branch .Lconv_entry

.LBB0_1496:
	s_cmp_lg_u32 s72, 3
	s_cbranch_scc1 .LBB0_1515
	s_branch .Lconv_entry

.LBB0_2167:
	s_or_b64 exec, exec, s[4:5]
	v_mov_b32_e32 v0, 0x2000
	v_mov_b32_e32 v1, 1
	s_waitcnt vmcnt(0)
	buffer_inv sc1
	global_atomic_add v0, v1, s[2:3] offset:1024
	s_waitcnt vmcnt(0)
